# SwiGLU gate/up epilogue regenerated: packed f32 mul/add, 8-wide stages, no serial chain
# baseline (speedup 1.0000x reference)
.LBB0_3276:
	s_mov_b32 s98, 0xbfb8aa3b
	s_mov_b32 s99, 0xbfb8aa3b
	v_mov_b32_e32 v166, 1.0
	v_mov_b32_e32 v167, 1.0
	v_lshl_add_u32 v140, s64, 8, v143
	s_lshl_b32 s19, s63, 7
	s_and_b32 s19, s19, 0x380
	v_ashrrev_i32_e32 v141, 31, v140
	v_lshlrev_b64 v[168:169], 11, v[140:141]
	v_lshl_add_u64 v[168:169], s[12:13], 0, v[168:169]
	v_or_b32_e32 v2, s19, v152
	v_lshlrev_b32_e32 v2, 1, v2
	v_lshl_add_u64 v[168:169], v[168:169], 0, v[2:3]
	v_pk_mul_f32 v[158:159], v[124:125], s[98:99]
	v_pk_mul_f32 v[160:161], v[126:127], s[98:99]
	v_pk_mul_f32 v[162:163], v[120:121], s[98:99]
	v_pk_mul_f32 v[164:165], v[122:123], s[98:99]
	v_exp_f32_e32 v158, v158
	v_exp_f32_e32 v159, v159
	v_exp_f32_e32 v160, v160
	v_exp_f32_e32 v161, v161
	v_exp_f32_e32 v162, v162
	v_exp_f32_e32 v163, v163
	v_exp_f32_e32 v164, v164
	v_exp_f32_e32 v165, v165
	v_pk_add_f32 v[158:159], v[158:159], v[166:167]
	v_pk_add_f32 v[160:161], v[160:161], v[166:167]
	v_pk_add_f32 v[162:163], v[162:163], v[166:167]
	v_pk_add_f32 v[164:165], v[164:165], v[166:167]
	v_rcp_f32_e32 v158, v158
	v_rcp_f32_e32 v159, v159
	v_rcp_f32_e32 v160, v160
	v_rcp_f32_e32 v161, v161
	v_rcp_f32_e32 v162, v162
	v_rcp_f32_e32 v163, v163
	v_rcp_f32_e32 v164, v164
	v_rcp_f32_e32 v165, v165
	v_pk_mul_f32 v[158:159], v[124:125], v[158:159]
	v_pk_mul_f32 v[160:161], v[126:127], v[160:161]
	v_pk_mul_f32 v[162:163], v[120:121], v[162:163]
	v_pk_mul_f32 v[164:165], v[122:123], v[164:165]
	v_pk_mul_f32 v[158:159], v[128:129], v[158:159]
	v_pk_mul_f32 v[160:161], v[130:131], v[160:161]
	v_pk_mul_f32 v[162:163], v[116:117], v[162:163]
	v_pk_mul_f32 v[164:165], v[118:119], v[164:165]
	v_cvt_pk_bf16_f32 v124, v158, v159
	v_cvt_pk_bf16_f32 v125, v160, v161
	v_cvt_pk_bf16_f32 v126, v162, v163
	v_cvt_pk_bf16_f32 v127, v164, v165
	global_store_dwordx4 v[168:169], v[124:127], off
	v_pk_mul_f32 v[158:159], v[112:113], s[98:99]
	v_pk_mul_f32 v[160:161], v[114:115], s[98:99]
	v_pk_mul_f32 v[162:163], v[104:105], s[98:99]
	v_pk_mul_f32 v[164:165], v[106:107], s[98:99]
	v_exp_f32_e32 v158, v158
	v_exp_f32_e32 v159, v159
	v_exp_f32_e32 v160, v160
	v_exp_f32_e32 v161, v161
	v_exp_f32_e32 v162, v162
	v_exp_f32_e32 v163, v163
	v_exp_f32_e32 v164, v164
	v_exp_f32_e32 v165, v165
	v_pk_add_f32 v[158:159], v[158:159], v[166:167]
	v_pk_add_f32 v[160:161], v[160:161], v[166:167]
	v_pk_add_f32 v[162:163], v[162:163], v[166:167]
	v_pk_add_f32 v[164:165], v[164:165], v[166:167]
	v_rcp_f32_e32 v158, v158
	v_rcp_f32_e32 v159, v159
	v_rcp_f32_e32 v160, v160
	v_rcp_f32_e32 v161, v161
	v_rcp_f32_e32 v162, v162
	v_rcp_f32_e32 v163, v163
	v_rcp_f32_e32 v164, v164
	v_rcp_f32_e32 v165, v165
	v_pk_mul_f32 v[158:159], v[112:113], v[158:159]
	v_pk_mul_f32 v[160:161], v[114:115], v[160:161]
	v_pk_mul_f32 v[162:163], v[104:105], v[162:163]
	v_pk_mul_f32 v[164:165], v[106:107], v[164:165]
	v_pk_mul_f32 v[158:159], v[108:109], v[158:159]
	v_pk_mul_f32 v[160:161], v[110:111], v[160:161]
	v_pk_mul_f32 v[162:163], v[100:101], v[162:163]
	v_pk_mul_f32 v[164:165], v[102:103], v[164:165]
	v_cvt_pk_bf16_f32 v112, v158, v159
	v_cvt_pk_bf16_f32 v113, v160, v161
	v_cvt_pk_bf16_f32 v114, v162, v163
	v_cvt_pk_bf16_f32 v115, v164, v165
	v_add_co_u32_e32 v108, vcc, 0x8000, v168
	s_nop 0
	v_addc_co_u32_e32 v109, vcc, 0, v169, vcc
	global_store_dwordx4 v[108:109], v[112:115], off
	v_pk_mul_f32 v[158:159], v[96:97], s[98:99]
	v_pk_mul_f32 v[160:161], v[98:99], s[98:99]
	v_pk_mul_f32 v[162:163], v[88:89], s[98:99]
	v_pk_mul_f32 v[164:165], v[90:91], s[98:99]
	v_exp_f32_e32 v158, v158
	v_exp_f32_e32 v159, v159
	v_exp_f32_e32 v160, v160
	v_exp_f32_e32 v161, v161
	v_exp_f32_e32 v162, v162
	v_exp_f32_e32 v163, v163
	v_exp_f32_e32 v164, v164
	v_exp_f32_e32 v165, v165
	v_pk_add_f32 v[158:159], v[158:159], v[166:167]
	v_pk_add_f32 v[160:161], v[160:161], v[166:167]
	v_pk_add_f32 v[162:163], v[162:163], v[166:167]
	v_pk_add_f32 v[164:165], v[164:165], v[166:167]
	v_rcp_f32_e32 v158, v158
	v_rcp_f32_e32 v159, v159
	v_rcp_f32_e32 v160, v160
	v_rcp_f32_e32 v161, v161
	v_rcp_f32_e32 v162, v162
	v_rcp_f32_e32 v163, v163
	v_rcp_f32_e32 v164, v164
	v_rcp_f32_e32 v165, v165
	v_pk_mul_f32 v[158:159], v[96:97], v[158:159]
	v_pk_mul_f32 v[160:161], v[98:99], v[160:161]
	v_pk_mul_f32 v[162:163], v[88:89], v[162:163]
	v_pk_mul_f32 v[164:165], v[90:91], v[164:165]
	v_pk_mul_f32 v[158:159], v[92:93], v[158:159]
	v_pk_mul_f32 v[160:161], v[94:95], v[160:161]
	v_pk_mul_f32 v[162:163], v[84:85], v[162:163]
	v_pk_mul_f32 v[164:165], v[86:87], v[164:165]
	v_cvt_pk_bf16_f32 v96, v158, v159
	v_cvt_pk_bf16_f32 v97, v160, v161
	v_cvt_pk_bf16_f32 v98, v162, v163
	v_cvt_pk_bf16_f32 v99, v164, v165
	v_add_co_u32_e32 v92, vcc, 0x10000, v168
	s_nop 0
	v_addc_co_u32_e32 v93, vcc, 0, v169, vcc
	global_store_dwordx4 v[92:93], v[96:99], off
	v_pk_mul_f32 v[158:159], v[80:81], s[98:99]
	v_pk_mul_f32 v[160:161], v[82:83], s[98:99]
	v_pk_mul_f32 v[162:163], v[72:73], s[98:99]
	v_pk_mul_f32 v[164:165], v[74:75], s[98:99]
	v_exp_f32_e32 v158, v158
	v_exp_f32_e32 v159, v159
	v_exp_f32_e32 v160, v160
	v_exp_f32_e32 v161, v161
	v_exp_f32_e32 v162, v162
	v_exp_f32_e32 v163, v163
	v_exp_f32_e32 v164, v164
	v_exp_f32_e32 v165, v165
	v_pk_add_f32 v[158:159], v[158:159], v[166:167]
	v_pk_add_f32 v[160:161], v[160:161], v[166:167]
	v_pk_add_f32 v[162:163], v[162:163], v[166:167]
	v_pk_add_f32 v[164:165], v[164:165], v[166:167]
	v_rcp_f32_e32 v158, v158
	v_rcp_f32_e32 v159, v159
	v_rcp_f32_e32 v160, v160
	v_rcp_f32_e32 v161, v161
	v_rcp_f32_e32 v162, v162
	v_rcp_f32_e32 v163, v163
	v_rcp_f32_e32 v164, v164
	v_rcp_f32_e32 v165, v165
	v_pk_mul_f32 v[158:159], v[80:81], v[158:159]
	v_pk_mul_f32 v[160:161], v[82:83], v[160:161]
	v_pk_mul_f32 v[162:163], v[72:73], v[162:163]
	v_pk_mul_f32 v[164:165], v[74:75], v[164:165]
	v_pk_mul_f32 v[158:159], v[76:77], v[158:159]
	v_pk_mul_f32 v[160:161], v[78:79], v[160:161]
	v_pk_mul_f32 v[162:163], v[68:69], v[162:163]
	v_pk_mul_f32 v[164:165], v[70:71], v[164:165]
	v_cvt_pk_bf16_f32 v80, v158, v159
	v_cvt_pk_bf16_f32 v81, v160, v161
	v_cvt_pk_bf16_f32 v82, v162, v163
	v_cvt_pk_bf16_f32 v83, v164, v165
	v_add_co_u32_e32 v76, vcc, 0x18000, v168
	s_nop 0
	v_addc_co_u32_e32 v77, vcc, 0, v169, vcc
	global_store_dwordx4 v[76:77], v[80:83], off
	v_pk_mul_f32 v[158:159], v[64:65], s[98:99]
	v_pk_mul_f32 v[160:161], v[66:67], s[98:99]
	v_pk_mul_f32 v[162:163], v[56:57], s[98:99]
	v_pk_mul_f32 v[164:165], v[58:59], s[98:99]
	v_exp_f32_e32 v158, v158
	v_exp_f32_e32 v159, v159
	v_exp_f32_e32 v160, v160
	v_exp_f32_e32 v161, v161
	v_exp_f32_e32 v162, v162
	v_exp_f32_e32 v163, v163
	v_exp_f32_e32 v164, v164
	v_exp_f32_e32 v165, v165
	v_pk_add_f32 v[158:159], v[158:159], v[166:167]
	v_pk_add_f32 v[160:161], v[160:161], v[166:167]
	v_pk_add_f32 v[162:163], v[162:163], v[166:167]
	v_pk_add_f32 v[164:165], v[164:165], v[166:167]
	v_rcp_f32_e32 v158, v158
	v_rcp_f32_e32 v159, v159
	v_rcp_f32_e32 v160, v160
	v_rcp_f32_e32 v161, v161
	v_rcp_f32_e32 v162, v162
	v_rcp_f32_e32 v163, v163
	v_rcp_f32_e32 v164, v164
	v_rcp_f32_e32 v165, v165
	v_pk_mul_f32 v[158:159], v[64:65], v[158:159]
	v_pk_mul_f32 v[160:161], v[66:67], v[160:161]
	v_pk_mul_f32 v[162:163], v[56:57], v[162:163]
	v_pk_mul_f32 v[164:165], v[58:59], v[164:165]
	v_pk_mul_f32 v[158:159], v[60:61], v[158:159]
	v_pk_mul_f32 v[160:161], v[62:63], v[160:161]
	v_pk_mul_f32 v[162:163], v[52:53], v[162:163]
	v_pk_mul_f32 v[164:165], v[54:55], v[164:165]
	v_cvt_pk_bf16_f32 v64, v158, v159
	v_cvt_pk_bf16_f32 v65, v160, v161
	v_cvt_pk_bf16_f32 v66, v162, v163
	v_cvt_pk_bf16_f32 v67, v164, v165
	v_add_co_u32_e32 v60, vcc, 0x40000, v168
	s_nop 0
	v_addc_co_u32_e32 v61, vcc, 0, v169, vcc
	global_store_dwordx4 v[60:61], v[64:67], off
	v_pk_mul_f32 v[158:159], v[48:49], s[98:99]
	v_pk_mul_f32 v[160:161], v[50:51], s[98:99]
	v_pk_mul_f32 v[162:163], v[40:41], s[98:99]
	v_pk_mul_f32 v[164:165], v[42:43], s[98:99]
	v_exp_f32_e32 v158, v158
	v_exp_f32_e32 v159, v159
	v_exp_f32_e32 v160, v160
	v_exp_f32_e32 v161, v161
	v_exp_f32_e32 v162, v162
	v_exp_f32_e32 v163, v163
	v_exp_f32_e32 v164, v164
	v_exp_f32_e32 v165, v165
	v_pk_add_f32 v[158:159], v[158:159], v[166:167]
	v_pk_add_f32 v[160:161], v[160:161], v[166:167]
	v_pk_add_f32 v[162:163], v[162:163], v[166:167]
	v_pk_add_f32 v[164:165], v[164:165], v[166:167]
	v_rcp_f32_e32 v158, v158
	v_rcp_f32_e32 v159, v159
	v_rcp_f32_e32 v160, v160
	v_rcp_f32_e32 v161, v161
	v_rcp_f32_e32 v162, v162
	v_rcp_f32_e32 v163, v163
	v_rcp_f32_e32 v164, v164
	v_rcp_f32_e32 v165, v165
	v_pk_mul_f32 v[158:159], v[48:49], v[158:159]
	v_pk_mul_f32 v[160:161], v[50:51], v[160:161]
	v_pk_mul_f32 v[162:163], v[40:41], v[162:163]
	v_pk_mul_f32 v[164:165], v[42:43], v[164:165]
	v_pk_mul_f32 v[158:159], v[44:45], v[158:159]
	v_pk_mul_f32 v[160:161], v[46:47], v[160:161]
	v_pk_mul_f32 v[162:163], v[36:37], v[162:163]
	v_pk_mul_f32 v[164:165], v[38:39], v[164:165]
	v_cvt_pk_bf16_f32 v48, v158, v159
	v_cvt_pk_bf16_f32 v49, v160, v161
	v_cvt_pk_bf16_f32 v50, v162, v163
	v_cvt_pk_bf16_f32 v51, v164, v165
	v_add_co_u32_e32 v44, vcc, 0x48000, v168
	s_nop 0
	v_addc_co_u32_e32 v45, vcc, 0, v169, vcc
	global_store_dwordx4 v[44:45], v[48:51], off
	v_pk_mul_f32 v[158:159], v[32:33], s[98:99]
	v_pk_mul_f32 v[160:161], v[34:35], s[98:99]
	v_pk_mul_f32 v[162:163], v[24:25], s[98:99]
	v_pk_mul_f32 v[164:165], v[26:27], s[98:99]
	v_exp_f32_e32 v158, v158
	v_exp_f32_e32 v159, v159
	v_exp_f32_e32 v160, v160
	v_exp_f32_e32 v161, v161
	v_exp_f32_e32 v162, v162
	v_exp_f32_e32 v163, v163
	v_exp_f32_e32 v164, v164
	v_exp_f32_e32 v165, v165
	v_pk_add_f32 v[158:159], v[158:159], v[166:167]
	v_pk_add_f32 v[160:161], v[160:161], v[166:167]
	v_pk_add_f32 v[162:163], v[162:163], v[166:167]
	v_pk_add_f32 v[164:165], v[164:165], v[166:167]
	v_rcp_f32_e32 v158, v158
	v_rcp_f32_e32 v159, v159
	v_rcp_f32_e32 v160, v160
	v_rcp_f32_e32 v161, v161
	v_rcp_f32_e32 v162, v162
	v_rcp_f32_e32 v163, v163
	v_rcp_f32_e32 v164, v164
	v_rcp_f32_e32 v165, v165
	v_pk_mul_f32 v[158:159], v[32:33], v[158:159]
	v_pk_mul_f32 v[160:161], v[34:35], v[160:161]
	v_pk_mul_f32 v[162:163], v[24:25], v[162:163]
	v_pk_mul_f32 v[164:165], v[26:27], v[164:165]
	v_pk_mul_f32 v[158:159], v[28:29], v[158:159]
	v_pk_mul_f32 v[160:161], v[30:31], v[160:161]
	v_pk_mul_f32 v[162:163], v[20:21], v[162:163]
	v_pk_mul_f32 v[164:165], v[22:23], v[164:165]
	v_cvt_pk_bf16_f32 v32, v158, v159
	v_cvt_pk_bf16_f32 v33, v160, v161
	v_cvt_pk_bf16_f32 v34, v162, v163
	v_cvt_pk_bf16_f32 v35, v164, v165
	v_add_co_u32_e32 v28, vcc, 0x50000, v168
	s_nop 0
	v_addc_co_u32_e32 v29, vcc, 0, v169, vcc
	global_store_dwordx4 v[28:29], v[32:35], off
	v_pk_mul_f32 v[158:159], v[16:17], s[98:99]
	v_pk_mul_f32 v[160:161], v[18:19], s[98:99]
	v_pk_mul_f32 v[162:163], v[8:9], s[98:99]
	v_pk_mul_f32 v[164:165], v[10:11], s[98:99]
	v_exp_f32_e32 v158, v158
	v_exp_f32_e32 v159, v159
	v_exp_f32_e32 v160, v160
	v_exp_f32_e32 v161, v161
	v_exp_f32_e32 v162, v162
	v_exp_f32_e32 v163, v163
	v_exp_f32_e32 v164, v164
	v_exp_f32_e32 v165, v165
	v_pk_add_f32 v[158:159], v[158:159], v[166:167]
	v_pk_add_f32 v[160:161], v[160:161], v[166:167]
	v_pk_add_f32 v[162:163], v[162:163], v[166:167]
	v_pk_add_f32 v[164:165], v[164:165], v[166:167]
	v_rcp_f32_e32 v158, v158
	v_rcp_f32_e32 v159, v159
	v_rcp_f32_e32 v160, v160
	v_rcp_f32_e32 v161, v161
	v_rcp_f32_e32 v162, v162
	v_rcp_f32_e32 v163, v163
	v_rcp_f32_e32 v164, v164
	v_rcp_f32_e32 v165, v165
	v_pk_mul_f32 v[158:159], v[16:17], v[158:159]
	v_pk_mul_f32 v[160:161], v[18:19], v[160:161]
	v_pk_mul_f32 v[162:163], v[8:9], v[162:163]
	v_pk_mul_f32 v[164:165], v[10:11], v[164:165]
	v_pk_mul_f32 v[158:159], v[12:13], v[158:159]
	v_pk_mul_f32 v[160:161], v[14:15], v[160:161]
	v_pk_mul_f32 v[162:163], v[4:5], v[162:163]
	v_pk_mul_f32 v[164:165], v[6:7], v[164:165]
	v_cvt_pk_bf16_f32 v16, v158, v159
	v_cvt_pk_bf16_f32 v17, v160, v161
	v_cvt_pk_bf16_f32 v18, v162, v163
	v_cvt_pk_bf16_f32 v19, v164, v165
	v_add_co_u32_e32 v12, vcc, 0x58000, v168
	s_nop 0
	v_addc_co_u32_e32 v13, vcc, 0, v169, vcc
	global_store_dwordx4 v[12:13], v[16:19], off
	s_and_b64 vcc, exec, s[38:39]
	s_cbranch_vccnz .LBB0_3281
	s_and_b64 vcc, exec, s[40:41]
	v_mov_b32_e32 v4, v157
	v_mov_b32_e32 v8, v154
	v_mov_b32_e32 v6, v156
	v_mov_b32_e32 v10, v155
	s_cbranch_vccnz .LBB0_3279
	s_waitcnt vmcnt(0)
	v_mad_u64_u32 v[4:5], s[20:21], v142, s48, v[132:133]
	v_mad_u64_u32 v[6:7], s[20:21], v145, s48, v[132:133]
	v_mad_u64_u32 v[8:9], s[20:21], v144, s48, v[134:135]
	v_mad_u64_u32 v[10:11], s[20:21], v146, s48, v[134:135]
